# baseline (speedup 1.0000x reference)
.LD_cdone1:
	s_waitcnt lgkmcnt(0)
	s_barrier
	v_mov_b32_e32 v252, 0x22000
	ds_read_b32 v200, v252
	ds_read_b32 v201, v252 offset:4
	ds_read_b32 v202, v252 offset:8
	s_waitcnt lgkmcnt(0)
	s_nop 1
	v_readfirstlane_b32 s31, v200
	v_readfirstlane_b32 s29, v201
	v_readfirstlane_b32 s30, v202
	s_nop 3
	s_barrier
	s_lshl_b32 s49, s29, 19
	s_lshl_b32 s64, s32, 13
	s_add_u32 s49, s49, s64
	s_mov_b32 s51, s64
	s_add_u32 s52, s51, 0x0
	s_add_u32 s53, s51, 0x1000
	s_add_u32 s54, s51, 0x8000
	s_add_u32 s55, s51, 0x9000
	s_add_u32 s56, s51, 0x10000
	s_add_u32 s57, s51, 0x11000
	s_add_u32 s58, s51, 0x18000
	s_add_u32 s59, s51, 0x19000
	s_lshl_b32 s64, s29, 8
	s_lshl_b32 s65, s30, 1
	s_add_u32 s64, s64, s65
	s_lshr_b32 s65, s32, 1
	s_add_u32 s64, s64, s65
	s_lshl_b32 s64, s64, 11
	s_and_b32 s65, s32, 1
	s_lshl_b32 s65, s65, 9
	s_add_u32 s50, s64, s65
	s_sub_u32 s60, s28, 1
	v_mov_b32_e32 v128, 0
	v_mov_b32_e32 v129, 0
	v_mov_b32_e32 v130, 0
	v_mov_b32_e32 v131, 0
	v_mov_b32_e32 v132, 0
	v_mov_b32_e32 v133, 0
	v_mov_b32_e32 v134, 0
	v_mov_b32_e32 v135, 0
	v_mov_b32_e32 v136, 0
	v_mov_b32_e32 v137, 0
	v_mov_b32_e32 v138, 0
	v_mov_b32_e32 v139, 0
	v_mov_b32_e32 v140, 0
	v_mov_b32_e32 v141, 0
	v_mov_b32_e32 v142, 0
	v_mov_b32_e32 v143, 0
	v_mov_b32_e32 v144, 0
	v_mov_b32_e32 v145, 0
	v_mov_b32_e32 v146, 0
	v_mov_b32_e32 v147, 0
	v_mov_b32_e32 v148, 0
	v_mov_b32_e32 v149, 0
	v_mov_b32_e32 v150, 0
	v_mov_b32_e32 v151, 0
	v_mov_b32_e32 v152, 0
	v_mov_b32_e32 v153, 0
	v_mov_b32_e32 v154, 0
	v_mov_b32_e32 v155, 0
	v_mov_b32_e32 v156, 0
	v_mov_b32_e32 v157, 0
	v_mov_b32_e32 v158, 0
	v_mov_b32_e32 v159, 0
	s_lshl_b32 s64, s30, 5
	s_lshl_b32 s65, s32, 3
	s_add_u32 s64, s64, s65
	v_lshlrev_b32_e32 v255, 2, v254
	v_add_u32_e32 v255, s64, v255
	v_lshlrev_b32_e32 v200, 2, v255
	global_load_dwordx4 v[228:231], v200, s[22:23]
	v_add_u32_e32 v201, 0x1000, v200
	global_load_dwordx4 v[232:235], v201, s[22:23]
	s_lshl_b32 s65, s32, 11
	v_lshl_add_u32 v248, v253, 3, s65
	v_add_u32_e32 v248, 0x20000, v248
	v_and_b32_e32 v250, 15, v194
	s_mul_i32 s65, s32, 128
	v_lshl_add_u32 v249, v250, 3, s65
	v_add_u32_e32 v249, 0x20000, v249
	v_lshlrev_b32_e32 v250, 3, v250
	s_lshl_b32 s65, s30, 11
	s_lshl_b32 s66, s29, 8
	s_add_u32 s65, s65, s66
	s_mul_i32 s66, s32, 16
	s_add_u32 s65, s65, s66
	s_lshl_b32 s65, s65, 3
	s_add_u32 s62, s24, s65
	s_addc_u32 s63, s25, 0
	s_lshl_b32 s65, s29, 5
	s_add_u32 s65, s65, s30
	s_lshl_b32 s65, s65, 2
	s_add_u32 s65, s65, s32
	s_lshl_b32 s65, s65, 15
	s_add_u32 s42, s18, s65
	s_addc_u32 s43, s19, 0
	s_waitcnt vmcnt(0)
	s_waitcnt vmcnt(0)
	s_mov_b32 s33, 0
	s_add_u32 s46, s42, 0x0
	s_addc_u32 s47, s43, 0
	global_load_dwordx4 v[0:3], v192, s[46:47] offset:0
	global_load_dwordx4 v[4:7], v192, s[46:47] offset:1024
	global_load_dwordx4 v[8:11], v192, s[46:47] offset:2048
	global_load_dwordx4 v[12:15], v192, s[46:47] offset:3072
	s_add_u32 s46, s42, 0x1000
	s_addc_u32 s47, s43, 0
	global_load_dwordx4 v[16:19], v192, s[46:47] offset:0
	global_load_dwordx4 v[20:23], v192, s[46:47] offset:1024
	global_load_dwordx4 v[24:27], v192, s[46:47] offset:2048
	global_load_dwordx4 v[28:31], v192, s[46:47] offset:3072
	s_add_u32 s46, s42, 0x2000
	s_addc_u32 s47, s43, 0
	global_load_dwordx4 v[32:35], v192, s[46:47] offset:0
	global_load_dwordx4 v[36:39], v192, s[46:47] offset:1024
	global_load_dwordx4 v[40:43], v192, s[46:47] offset:2048
	global_load_dwordx4 v[44:47], v192, s[46:47] offset:3072
	s_add_u32 s46, s42, 0x3000
	s_addc_u32 s47, s43, 0
	global_load_dwordx4 v[48:51], v192, s[46:47] offset:0
	global_load_dwordx4 v[52:55], v192, s[46:47] offset:1024
	global_load_dwordx4 v[56:59], v192, s[46:47] offset:2048
	global_load_dwordx4 v[60:63], v192, s[46:47] offset:3072
	s_add_u32 s46, s42, 0x4000
	s_addc_u32 s47, s43, 0
	global_load_dwordx4 v[64:67], v192, s[46:47] offset:0
	global_load_dwordx4 v[68:71], v192, s[46:47] offset:1024
	global_load_dwordx4 v[72:75], v192, s[46:47] offset:2048
	global_load_dwordx4 v[76:79], v192, s[46:47] offset:3072
	s_add_u32 s46, s42, 0x5000
	s_addc_u32 s47, s43, 0
	global_load_dwordx4 v[80:83], v192, s[46:47] offset:0
	global_load_dwordx4 v[84:87], v192, s[46:47] offset:1024
	global_load_dwordx4 v[88:91], v192, s[46:47] offset:2048
	global_load_dwordx4 v[92:95], v192, s[46:47] offset:3072
	s_add_u32 s46, s42, 0x6000
	s_addc_u32 s47, s43, 0
	global_load_dwordx4 v[96:99], v192, s[46:47] offset:0
	global_load_dwordx4 v[100:103], v192, s[46:47] offset:1024
	global_load_dwordx4 v[104:107], v192, s[46:47] offset:2048
	global_load_dwordx4 v[108:111], v192, s[46:47] offset:3072
	s_add_u32 s46, s42, 0x7000
	s_addc_u32 s47, s43, 0
	global_load_dwordx4 v[112:115], v192, s[46:47] offset:0
	global_load_dwordx4 v[116:119], v192, s[46:47] offset:1024
	global_load_dwordx4 v[120:123], v192, s[46:47] offset:2048
	global_load_dwordx4 v[124:127], v192, s[46:47] offset:3072
	s_waitcnt vmcnt(0)
	s_waitcnt lgkmcnt(0)
	s_lshl_b32 s64, s30, 2
	s_add_u32 s64, s64, s32
	s_lshl_b32 s64, s64, 16
	s_add_u32 s44, s4, s64
	s_addc_u32 s45, s5, 0
	global_load_dwordx4 a[0:3], v192, s[44:45] offset:0
	global_load_dwordx4 a[4:7], v192, s[44:45] offset:1024
	global_load_dwordx4 a[8:11], v192, s[44:45] offset:2048
	global_load_dwordx4 a[12:15], v192, s[44:45] offset:3072
	s_add_u32 s44, s44, 0x1000
	s_addc_u32 s45, s45, 0
	global_load_dwordx4 a[16:19], v192, s[44:45] offset:0
	global_load_dwordx4 a[20:23], v192, s[44:45] offset:1024
	global_load_dwordx4 a[24:27], v192, s[44:45] offset:2048
	global_load_dwordx4 a[28:31], v192, s[44:45] offset:3072
	s_add_u32 s44, s44, 0x1000
	s_addc_u32 s45, s45, 0
	global_load_dwordx4 a[32:35], v192, s[44:45] offset:0
	global_load_dwordx4 a[36:39], v192, s[44:45] offset:1024
	global_load_dwordx4 a[40:43], v192, s[44:45] offset:2048
	global_load_dwordx4 a[44:47], v192, s[44:45] offset:3072
	s_add_u32 s44, s44, 0x1000
	s_addc_u32 s45, s45, 0
	global_load_dwordx4 a[48:51], v192, s[44:45] offset:0
	global_load_dwordx4 a[52:55], v192, s[44:45] offset:1024
	global_load_dwordx4 a[56:59], v192, s[44:45] offset:2048
	global_load_dwordx4 a[60:63], v192, s[44:45] offset:3072
	s_add_u32 s44, s44, 0x1000
	s_addc_u32 s45, s45, 0
	global_load_dwordx4 a[64:67], v192, s[44:45] offset:0
	global_load_dwordx4 a[68:71], v192, s[44:45] offset:1024
	global_load_dwordx4 a[72:75], v192, s[44:45] offset:2048
	global_load_dwordx4 a[76:79], v192, s[44:45] offset:3072
	s_add_u32 s44, s44, 0x1000
	s_addc_u32 s45, s45, 0
	global_load_dwordx4 a[80:83], v192, s[44:45] offset:0
	global_load_dwordx4 a[84:87], v192, s[44:45] offset:1024
	global_load_dwordx4 a[88:91], v192, s[44:45] offset:2048
	global_load_dwordx4 a[92:95], v192, s[44:45] offset:3072
	s_add_u32 s44, s44, 0x1000
	s_addc_u32 s45, s45, 0
	global_load_dwordx4 a[96:99], v192, s[44:45] offset:0
	global_load_dwordx4 a[100:103], v192, s[44:45] offset:1024
	global_load_dwordx4 a[104:107], v192, s[44:45] offset:2048
	global_load_dwordx4 a[108:111], v192, s[44:45] offset:3072
	s_add_u32 s44, s44, 0x1000
	s_addc_u32 s45, s45, 0
	global_load_dwordx4 a[112:115], v192, s[44:45] offset:0
	global_load_dwordx4 a[116:119], v192, s[44:45] offset:1024
	global_load_dwordx4 a[120:123], v192, s[44:45] offset:2048
	global_load_dwordx4 a[124:127], v192, s[44:45] offset:3072
	s_add_u32 s44, s44, 0x1000
	s_addc_u32 s45, s45, 0
	s_waitcnt vmcnt(16)
	global_load_dwordx4 a[128:131], v192, s[44:45] offset:0
	global_load_dwordx4 a[132:135], v192, s[44:45] offset:1024
	global_load_dwordx4 a[136:139], v192, s[44:45] offset:2048
	global_load_dwordx4 a[140:143], v192, s[44:45] offset:3072
	s_add_u32 s44, s44, 0x1000
	s_addc_u32 s45, s45, 0
	global_load_dwordx4 a[144:147], v192, s[44:45] offset:0
	global_load_dwordx4 a[148:151], v192, s[44:45] offset:1024
	global_load_dwordx4 a[152:155], v192, s[44:45] offset:2048
	global_load_dwordx4 a[156:159], v192, s[44:45] offset:3072
	s_add_u32 s44, s44, 0x1000
	s_addc_u32 s45, s45, 0
	global_load_dwordx4 a[160:163], v192, s[44:45] offset:0
	global_load_dwordx4 a[164:167], v192, s[44:45] offset:1024
	global_load_dwordx4 a[168:171], v192, s[44:45] offset:2048
	global_load_dwordx4 a[172:175], v192, s[44:45] offset:3072
	s_add_u32 s44, s44, 0x1000
	s_addc_u32 s45, s45, 0
	global_load_dwordx4 a[176:179], v192, s[44:45] offset:0
	global_load_dwordx4 a[180:183], v192, s[44:45] offset:1024
	global_load_dwordx4 a[184:187], v192, s[44:45] offset:2048
	global_load_dwordx4 a[188:191], v192, s[44:45] offset:3072
	s_add_u32 s44, s44, 0x1000
	s_addc_u32 s45, s45, 0
	global_load_dwordx4 a[192:195], v192, s[44:45] offset:0
	global_load_dwordx4 a[196:199], v192, s[44:45] offset:1024
	global_load_dwordx4 a[200:203], v192, s[44:45] offset:2048
	global_load_dwordx4 a[204:207], v192, s[44:45] offset:3072
	s_add_u32 s44, s44, 0x1000
	s_addc_u32 s45, s45, 0
	global_load_dwordx4 a[208:211], v192, s[44:45] offset:0
	global_load_dwordx4 a[212:215], v192, s[44:45] offset:1024
	global_load_dwordx4 a[216:219], v192, s[44:45] offset:2048
	global_load_dwordx4 a[220:223], v192, s[44:45] offset:3072
	s_add_u32 s44, s44, 0x1000
	s_addc_u32 s45, s45, 0
	global_load_dwordx4 a[224:227], v192, s[44:45] offset:0
	global_load_dwordx4 a[228:231], v192, s[44:45] offset:1024
	global_load_dwordx4 a[232:235], v192, s[44:45] offset:2048
	global_load_dwordx4 a[236:239], v192, s[44:45] offset:3072
	s_add_u32 s44, s44, 0x1000
	s_addc_u32 s45, s45, 0
	global_load_dwordx4 a[240:243], v192, s[44:45] offset:0
	global_load_dwordx4 a[244:247], v192, s[44:45] offset:1024
	global_load_dwordx4 a[248:251], v192, s[44:45] offset:2048
	global_load_dwordx4 a[252:255], v192, s[44:45] offset:3072
	s_add_u32 s44, s44, 0x1000
	s_addc_u32 s45, s45, 0
	s_lshl_b32 s64, s33, 3
	s_add_u32 s64, s64, s29
	s_lshl_b32 s64, s64, 5
	s_add_u32 s64, s64, s30
	s_lshl_b32 s64, s64, 2
	s_add_u32 s40, s8, s64
	s_addc_u32 s41, s9, 0
	s_and_b32 s64, s33, 1
	s_lshl_b32 s64, s64, 22
	s_add_u32 s64, s64, s50
	s_add_u32 s36, s6, s64
	s_addc_u32 s37, s7, 0
	v_exp_f32_e32 v200, v0
	v_exp_f32_e32 v201, v1
	v_exp_f32_e32 v202, v2
	v_exp_f32_e32 v203, v3
	v_exp_f32_e32 v204, v4
	v_exp_f32_e32 v205, v5
	v_exp_f32_e32 v206, v6
	v_exp_f32_e32 v207, v7
	v_exp_f32_e32 v208, v8
	v_exp_f32_e32 v209, v9
	v_exp_f32_e32 v210, v10
	v_exp_f32_e32 v211, v11
	v_exp_f32_e32 v212, v12
	v_exp_f32_e32 v213, v13
	v_exp_f32_e32 v214, v14
	v_exp_f32_e32 v215, v15
	v_add_f32_e32 v200, 1.0, v200
	v_add_f32_e32 v201, 1.0, v201
	v_add_f32_e32 v202, 1.0, v202
	v_add_f32_e32 v203, 1.0, v203
	v_add_f32_e32 v204, 1.0, v204
	v_add_f32_e32 v205, 1.0, v205
	v_add_f32_e32 v206, 1.0, v206
	v_add_f32_e32 v207, 1.0, v207
	v_add_f32_e32 v208, 1.0, v208
	v_add_f32_e32 v209, 1.0, v209
	v_add_f32_e32 v210, 1.0, v210
	v_add_f32_e32 v211, 1.0, v211
	v_add_f32_e32 v212, 1.0, v212
	v_add_f32_e32 v213, 1.0, v213
	v_add_f32_e32 v214, 1.0, v214
	v_add_f32_e32 v215, 1.0, v215
	v_rcp_f32_e32 v200, v200
	v_rcp_f32_e32 v201, v201
	v_rcp_f32_e32 v202, v202
	v_rcp_f32_e32 v203, v203
	v_rcp_f32_e32 v204, v204
	v_rcp_f32_e32 v205, v205
	v_rcp_f32_e32 v206, v206
	v_rcp_f32_e32 v207, v207
	v_rcp_f32_e32 v208, v208
	v_rcp_f32_e32 v209, v209
	v_rcp_f32_e32 v210, v210
	v_rcp_f32_e32 v211, v211
	v_rcp_f32_e32 v212, v212
	v_rcp_f32_e32 v213, v213
	v_rcp_f32_e32 v214, v214
	v_rcp_f32_e32 v215, v215
	v_fmamk_f32 v208, v208, 0xc0b8aa3b, v198
	v_fmamk_f32 v209, v209, 0xc0b8aa3b, v198
	v_fmamk_f32 v210, v210, 0xc0b8aa3b, v198
	v_fmamk_f32 v211, v211, 0xc0b8aa3b, v198
	v_mul_f32_e32 v204, v204, v128
	v_mul_f32_e32 v205, v205, v129
	v_mul_f32_e32 v206, v206, v130
	v_mul_f32_e32 v207, v207, v131
	v_fma_f32 v128, v200, v208, v204
	v_fma_f32 v129, v201, v209, v205
	v_fma_f32 v130, v202, v210, v206
	v_fma_f32 v131, v203, v211, v207
	v_exp_f32_e32 v200, v128
	v_exp_f32_e32 v201, v129
	v_exp_f32_e32 v202, v130
	v_exp_f32_e32 v203, v131
	v_add_f32_e32 v200, 1.0, v200
	v_add_f32_e32 v201, 1.0, v201
	v_add_f32_e32 v202, 1.0, v202
	v_add_f32_e32 v203, 1.0, v203
	v_rcp_f32_e32 v200, v200
	v_rcp_f32_e32 v201, v201
	v_rcp_f32_e32 v202, v202
	v_rcp_f32_e32 v203, v203
	v_fma_f32 v200, v200, 2.0, -1.0
	v_fma_f32 v201, v201, 2.0, -1.0
	v_fma_f32 v202, v202, 2.0, -1.0
	v_fma_f32 v203, v203, 2.0, -1.0
	v_mul_f32_e32 v216, v212, v200
	v_mul_f32_e32 v217, v213, v201
	v_mul_f32_e32 v218, v214, v202
	v_mul_f32_e32 v219, v215, v203
	v_mul_f32_e32 v236, v216, v228
	v_mul_f32_e32 v237, v216, v232
	v_fmac_f32_e32 v236, v217, v229
	v_fmac_f32_e32 v237, v217, v233
	v_fmac_f32_e32 v236, v218, v230
	v_fmac_f32_e32 v237, v218, v234
	v_fmac_f32_e32 v236, v219, v231
	v_fmac_f32_e32 v237, v219, v235
	v_mov_b32_e32 v238, v236
	v_mov_b32_e32 v239, v236
	v_mov_b32_e32 v240, v237
	v_mov_b32_e32 v241, v237
	s_nop 1
	v_permlane32_swap_b32_e32 v238, v239
	v_permlane32_swap_b32_e32 v240, v241
	v_add_f32_e32 v238, v238, v239
	v_add_f32_e32 v239, v240, v241
	ds_write_b64 v248, v[238:239] offset:0
	v_cvt_pk_f16_f32 v220, v216, v217
	v_cvt_pk_f16_f32 v221, v218, v219
	v_exp_f32_e32 v200, v16
	v_exp_f32_e32 v201, v17
	v_exp_f32_e32 v202, v18
	v_exp_f32_e32 v203, v19
	v_exp_f32_e32 v204, v20
	v_exp_f32_e32 v205, v21
	v_exp_f32_e32 v206, v22
	v_exp_f32_e32 v207, v23
	v_exp_f32_e32 v208, v24
	v_exp_f32_e32 v209, v25
	v_exp_f32_e32 v210, v26
	v_exp_f32_e32 v211, v27
	v_exp_f32_e32 v212, v28
	v_exp_f32_e32 v213, v29
	v_exp_f32_e32 v214, v30
	v_exp_f32_e32 v215, v31
	v_add_f32_e32 v200, 1.0, v200
	v_add_f32_e32 v201, 1.0, v201
	v_add_f32_e32 v202, 1.0, v202
	v_add_f32_e32 v203, 1.0, v203
	v_add_f32_e32 v204, 1.0, v204
	v_add_f32_e32 v205, 1.0, v205
	v_add_f32_e32 v206, 1.0, v206
	v_add_f32_e32 v207, 1.0, v207
	v_add_f32_e32 v208, 1.0, v208
	v_add_f32_e32 v209, 1.0, v209
	v_add_f32_e32 v210, 1.0, v210
	v_add_f32_e32 v211, 1.0, v211
	v_add_f32_e32 v212, 1.0, v212
	v_add_f32_e32 v213, 1.0, v213
	v_add_f32_e32 v214, 1.0, v214
	v_add_f32_e32 v215, 1.0, v215
	v_rcp_f32_e32 v200, v200
	v_rcp_f32_e32 v201, v201
	v_rcp_f32_e32 v202, v202
	v_rcp_f32_e32 v203, v203
	v_rcp_f32_e32 v204, v204
	v_rcp_f32_e32 v205, v205
	v_rcp_f32_e32 v206, v206
	v_rcp_f32_e32 v207, v207
	v_rcp_f32_e32 v208, v208
	v_rcp_f32_e32 v209, v209
	v_rcp_f32_e32 v210, v210
	v_rcp_f32_e32 v211, v211
	v_rcp_f32_e32 v212, v212
	v_rcp_f32_e32 v213, v213
	v_rcp_f32_e32 v214, v214
	v_rcp_f32_e32 v215, v215
	v_fmamk_f32 v208, v208, 0xc0b8aa3b, v198
	v_fmamk_f32 v209, v209, 0xc0b8aa3b, v198
	v_fmamk_f32 v210, v210, 0xc0b8aa3b, v198
	v_fmamk_f32 v211, v211, 0xc0b8aa3b, v198
	v_mul_f32_e32 v204, v204, v132
	v_mul_f32_e32 v205, v205, v133
	v_mul_f32_e32 v206, v206, v134
	v_mul_f32_e32 v207, v207, v135
	v_fma_f32 v132, v200, v208, v204
	v_fma_f32 v133, v201, v209, v205
	v_fma_f32 v134, v202, v210, v206
	v_fma_f32 v135, v203, v211, v207
	v_exp_f32_e32 v200, v132
	v_exp_f32_e32 v201, v133
	v_exp_f32_e32 v202, v134
	v_exp_f32_e32 v203, v135
	v_add_f32_e32 v200, 1.0, v200
	v_add_f32_e32 v201, 1.0, v201
	v_add_f32_e32 v202, 1.0, v202
	v_add_f32_e32 v203, 1.0, v203
	v_rcp_f32_e32 v200, v200
	v_rcp_f32_e32 v201, v201
	v_rcp_f32_e32 v202, v202
	v_rcp_f32_e32 v203, v203
	v_fma_f32 v200, v200, 2.0, -1.0
	v_fma_f32 v201, v201, 2.0, -1.0
	v_fma_f32 v202, v202, 2.0, -1.0
	v_fma_f32 v203, v203, 2.0, -1.0
	v_mul_f32_e32 v216, v212, v200
	v_mul_f32_e32 v217, v213, v201
	v_mul_f32_e32 v218, v214, v202
	v_mul_f32_e32 v219, v215, v203
	v_mul_f32_e32 v236, v216, v228
	v_mul_f32_e32 v237, v216, v232
	v_fmac_f32_e32 v236, v217, v229
	v_fmac_f32_e32 v237, v217, v233
	v_fmac_f32_e32 v236, v218, v230
	v_fmac_f32_e32 v237, v218, v234
	v_fmac_f32_e32 v236, v219, v231
	v_fmac_f32_e32 v237, v219, v235
	v_mov_b32_e32 v238, v236
	v_mov_b32_e32 v239, v236
	v_mov_b32_e32 v240, v237
	v_mov_b32_e32 v241, v237
	s_nop 1
	v_permlane32_swap_b32_e32 v238, v239
	v_permlane32_swap_b32_e32 v240, v241
	v_add_f32_e32 v238, v238, v239
	v_add_f32_e32 v239, v240, v241
	ds_write_b64 v248, v[238:239] offset:256
	v_cvt_pk_f16_f32 v222, v216, v217
	v_cvt_pk_f16_f32 v223, v218, v219
	s_nop 1
	v_permlane32_swap_b32_e32 v220, v222
	v_permlane32_swap_b32_e32 v221, v223
	s_cmp_eq_u32 s31, 0
	s_cbranch_scc1 .LD_slow4
	global_store_dwordx4 v195, v[220:223], s[36:37] offset:0
.LD_join5:
	s_and_b32 s64, s33, 1
	s_lshl_b32 s64, s64, 22
	s_add_u32 s64, s64, s50
	s_add_u32 s64, s64, 0x20000
	s_add_u32 s36, s6, s64
	s_addc_u32 s37, s7, 0
	v_exp_f32_e32 v200, v32
	v_exp_f32_e32 v201, v33
	v_exp_f32_e32 v202, v34
	v_exp_f32_e32 v203, v35
	v_exp_f32_e32 v204, v36
	v_exp_f32_e32 v205, v37
	v_exp_f32_e32 v206, v38
	v_exp_f32_e32 v207, v39
	v_exp_f32_e32 v208, v40
	v_exp_f32_e32 v209, v41
	v_exp_f32_e32 v210, v42
	v_exp_f32_e32 v211, v43
	v_exp_f32_e32 v212, v44
	v_exp_f32_e32 v213, v45
	v_exp_f32_e32 v214, v46
	v_exp_f32_e32 v215, v47
	v_add_f32_e32 v200, 1.0, v200
	v_add_f32_e32 v201, 1.0, v201
	v_add_f32_e32 v202, 1.0, v202
	v_add_f32_e32 v203, 1.0, v203
	v_add_f32_e32 v204, 1.0, v204
	v_add_f32_e32 v205, 1.0, v205
	v_add_f32_e32 v206, 1.0, v206
	v_add_f32_e32 v207, 1.0, v207
	v_add_f32_e32 v208, 1.0, v208
	v_add_f32_e32 v209, 1.0, v209
	v_add_f32_e32 v210, 1.0, v210
	v_add_f32_e32 v211, 1.0, v211
	v_add_f32_e32 v212, 1.0, v212
	v_add_f32_e32 v213, 1.0, v213
	v_add_f32_e32 v214, 1.0, v214
	v_add_f32_e32 v215, 1.0, v215
	v_rcp_f32_e32 v200, v200
	v_rcp_f32_e32 v201, v201
	v_rcp_f32_e32 v202, v202
	v_rcp_f32_e32 v203, v203
	v_rcp_f32_e32 v204, v204
	v_rcp_f32_e32 v205, v205
	v_rcp_f32_e32 v206, v206
	v_rcp_f32_e32 v207, v207
	v_rcp_f32_e32 v208, v208
	v_rcp_f32_e32 v209, v209
	v_rcp_f32_e32 v210, v210
	v_rcp_f32_e32 v211, v211
	v_rcp_f32_e32 v212, v212
	v_rcp_f32_e32 v213, v213
	v_rcp_f32_e32 v214, v214
	v_rcp_f32_e32 v215, v215
	v_fmamk_f32 v208, v208, 0xc0b8aa3b, v198
	v_fmamk_f32 v209, v209, 0xc0b8aa3b, v198
	v_fmamk_f32 v210, v210, 0xc0b8aa3b, v198
	v_fmamk_f32 v211, v211, 0xc0b8aa3b, v198
	v_mul_f32_e32 v204, v204, v136
	v_mul_f32_e32 v205, v205, v137
	v_mul_f32_e32 v206, v206, v138
	v_mul_f32_e32 v207, v207, v139
	v_fma_f32 v136, v200, v208, v204
	v_fma_f32 v137, v201, v209, v205
	v_fma_f32 v138, v202, v210, v206
	v_fma_f32 v139, v203, v211, v207
	v_exp_f32_e32 v200, v136
	v_exp_f32_e32 v201, v137
	v_exp_f32_e32 v202, v138
	v_exp_f32_e32 v203, v139
	v_add_f32_e32 v200, 1.0, v200
	v_add_f32_e32 v201, 1.0, v201
	v_add_f32_e32 v202, 1.0, v202
	v_add_f32_e32 v203, 1.0, v203
	v_rcp_f32_e32 v200, v200
	v_rcp_f32_e32 v201, v201
	v_rcp_f32_e32 v202, v202
	v_rcp_f32_e32 v203, v203
	v_fma_f32 v200, v200, 2.0, -1.0
	v_fma_f32 v201, v201, 2.0, -1.0
	v_fma_f32 v202, v202, 2.0, -1.0
	v_fma_f32 v203, v203, 2.0, -1.0
	v_mul_f32_e32 v216, v212, v200
	v_mul_f32_e32 v217, v213, v201
	v_mul_f32_e32 v218, v214, v202
	v_mul_f32_e32 v219, v215, v203
	v_mul_f32_e32 v236, v216, v228
	v_mul_f32_e32 v237, v216, v232
	v_fmac_f32_e32 v236, v217, v229
	v_fmac_f32_e32 v237, v217, v233
	v_fmac_f32_e32 v236, v218, v230
	v_fmac_f32_e32 v237, v218, v234
	v_fmac_f32_e32 v236, v219, v231
	v_fmac_f32_e32 v237, v219, v235
	v_mov_b32_e32 v238, v236
	v_mov_b32_e32 v239, v236
	v_mov_b32_e32 v240, v237
	v_mov_b32_e32 v241, v237
	s_nop 1
	v_permlane32_swap_b32_e32 v238, v239
	v_permlane32_swap_b32_e32 v240, v241
	v_add_f32_e32 v238, v238, v239
	v_add_f32_e32 v239, v240, v241
	ds_write_b64 v248, v[238:239] offset:512
	v_cvt_pk_f16_f32 v220, v216, v217
	v_cvt_pk_f16_f32 v221, v218, v219
	v_exp_f32_e32 v200, v48
	v_exp_f32_e32 v201, v49
	v_exp_f32_e32 v202, v50
	v_exp_f32_e32 v203, v51
	v_exp_f32_e32 v204, v52
	v_exp_f32_e32 v205, v53
	v_exp_f32_e32 v206, v54
	v_exp_f32_e32 v207, v55
	v_exp_f32_e32 v208, v56
	v_exp_f32_e32 v209, v57
	v_exp_f32_e32 v210, v58
	v_exp_f32_e32 v211, v59
	v_exp_f32_e32 v212, v60
	v_exp_f32_e32 v213, v61
	v_exp_f32_e32 v214, v62
	v_exp_f32_e32 v215, v63
	v_add_f32_e32 v200, 1.0, v200
	v_add_f32_e32 v201, 1.0, v201
	v_add_f32_e32 v202, 1.0, v202
	v_add_f32_e32 v203, 1.0, v203
	v_add_f32_e32 v204, 1.0, v204
	v_add_f32_e32 v205, 1.0, v205
	v_add_f32_e32 v206, 1.0, v206
	v_add_f32_e32 v207, 1.0, v207
	v_add_f32_e32 v208, 1.0, v208
	v_add_f32_e32 v209, 1.0, v209
	v_add_f32_e32 v210, 1.0, v210
	v_add_f32_e32 v211, 1.0, v211
	v_add_f32_e32 v212, 1.0, v212
	v_add_f32_e32 v213, 1.0, v213
	v_add_f32_e32 v214, 1.0, v214
	v_add_f32_e32 v215, 1.0, v215
	v_rcp_f32_e32 v200, v200
	v_rcp_f32_e32 v201, v201
	v_rcp_f32_e32 v202, v202
	v_rcp_f32_e32 v203, v203
	v_rcp_f32_e32 v204, v204
	v_rcp_f32_e32 v205, v205
	v_rcp_f32_e32 v206, v206
	v_rcp_f32_e32 v207, v207
	v_rcp_f32_e32 v208, v208
	v_rcp_f32_e32 v209, v209
	v_rcp_f32_e32 v210, v210
	v_rcp_f32_e32 v211, v211
	v_rcp_f32_e32 v212, v212
	v_rcp_f32_e32 v213, v213
	v_rcp_f32_e32 v214, v214
	v_rcp_f32_e32 v215, v215
	v_fmamk_f32 v208, v208, 0xc0b8aa3b, v198
	v_fmamk_f32 v209, v209, 0xc0b8aa3b, v198
	v_fmamk_f32 v210, v210, 0xc0b8aa3b, v198
	v_fmamk_f32 v211, v211, 0xc0b8aa3b, v198
	v_mul_f32_e32 v204, v204, v140
	v_mul_f32_e32 v205, v205, v141
	v_mul_f32_e32 v206, v206, v142
	v_mul_f32_e32 v207, v207, v143
	v_fma_f32 v140, v200, v208, v204
	v_fma_f32 v141, v201, v209, v205
	v_fma_f32 v142, v202, v210, v206
	v_fma_f32 v143, v203, v211, v207
	v_exp_f32_e32 v200, v140
	v_exp_f32_e32 v201, v141
	v_exp_f32_e32 v202, v142
	v_exp_f32_e32 v203, v143
	v_add_f32_e32 v200, 1.0, v200
	v_add_f32_e32 v201, 1.0, v201
	v_add_f32_e32 v202, 1.0, v202
	v_add_f32_e32 v203, 1.0, v203
	v_rcp_f32_e32 v200, v200
	v_rcp_f32_e32 v201, v201
	v_rcp_f32_e32 v202, v202
	v_rcp_f32_e32 v203, v203
	v_fma_f32 v200, v200, 2.0, -1.0
	v_fma_f32 v201, v201, 2.0, -1.0
	v_fma_f32 v202, v202, 2.0, -1.0
	v_fma_f32 v203, v203, 2.0, -1.0
	v_mul_f32_e32 v216, v212, v200
	v_mul_f32_e32 v217, v213, v201
	v_mul_f32_e32 v218, v214, v202
	v_mul_f32_e32 v219, v215, v203
	v_mul_f32_e32 v236, v216, v228
	v_mul_f32_e32 v237, v216, v232
	v_fmac_f32_e32 v236, v217, v229
	v_fmac_f32_e32 v237, v217, v233
	v_fmac_f32_e32 v236, v218, v230
	v_fmac_f32_e32 v237, v218, v234
	v_fmac_f32_e32 v236, v219, v231
	v_fmac_f32_e32 v237, v219, v235
	v_mov_b32_e32 v238, v236
	v_mov_b32_e32 v239, v236
	v_mov_b32_e32 v240, v237
	v_mov_b32_e32 v241, v237
	s_nop 1
	v_permlane32_swap_b32_e32 v238, v239
	v_permlane32_swap_b32_e32 v240, v241
	v_add_f32_e32 v238, v238, v239
	v_add_f32_e32 v239, v240, v241
	ds_write_b64 v248, v[238:239] offset:768
	v_cvt_pk_f16_f32 v222, v216, v217
	v_cvt_pk_f16_f32 v223, v218, v219
	s_nop 1
	v_permlane32_swap_b32_e32 v220, v222
	v_permlane32_swap_b32_e32 v221, v223
	s_cmp_eq_u32 s31, 0
	s_cbranch_scc1 .LD_slow6
	global_store_dwordx4 v195, v[220:223], s[36:37] offset:0
.LD_join7:
	s_and_b32 s64, s33, 1
	s_lshl_b32 s64, s64, 22
	s_add_u32 s64, s64, s50
	s_add_u32 s64, s64, 0x40000
	s_add_u32 s36, s6, s64
	s_addc_u32 s37, s7, 0
	v_exp_f32_e32 v200, v64
	v_exp_f32_e32 v201, v65
	v_exp_f32_e32 v202, v66
	v_exp_f32_e32 v203, v67
	v_exp_f32_e32 v204, v68
	v_exp_f32_e32 v205, v69
	v_exp_f32_e32 v206, v70
	v_exp_f32_e32 v207, v71
	v_exp_f32_e32 v208, v72
	v_exp_f32_e32 v209, v73
	v_exp_f32_e32 v210, v74
	v_exp_f32_e32 v211, v75
	v_exp_f32_e32 v212, v76
	v_exp_f32_e32 v213, v77
	v_exp_f32_e32 v214, v78
	v_exp_f32_e32 v215, v79
	v_add_f32_e32 v200, 1.0, v200
	v_add_f32_e32 v201, 1.0, v201
	v_add_f32_e32 v202, 1.0, v202
	v_add_f32_e32 v203, 1.0, v203
	v_add_f32_e32 v204, 1.0, v204
	v_add_f32_e32 v205, 1.0, v205
	v_add_f32_e32 v206, 1.0, v206
	v_add_f32_e32 v207, 1.0, v207
	v_add_f32_e32 v208, 1.0, v208
	v_add_f32_e32 v209, 1.0, v209
	v_add_f32_e32 v210, 1.0, v210
	v_add_f32_e32 v211, 1.0, v211
	v_add_f32_e32 v212, 1.0, v212
	v_add_f32_e32 v213, 1.0, v213
	v_add_f32_e32 v214, 1.0, v214
	v_add_f32_e32 v215, 1.0, v215
	v_rcp_f32_e32 v200, v200
	v_rcp_f32_e32 v201, v201
	v_rcp_f32_e32 v202, v202
	v_rcp_f32_e32 v203, v203
	v_rcp_f32_e32 v204, v204
	v_rcp_f32_e32 v205, v205
	v_rcp_f32_e32 v206, v206
	v_rcp_f32_e32 v207, v207
	v_rcp_f32_e32 v208, v208
	v_rcp_f32_e32 v209, v209
	v_rcp_f32_e32 v210, v210
	v_rcp_f32_e32 v211, v211
	v_rcp_f32_e32 v212, v212
	v_rcp_f32_e32 v213, v213
	v_rcp_f32_e32 v214, v214
	v_rcp_f32_e32 v215, v215
	v_fmamk_f32 v208, v208, 0xc0b8aa3b, v198
	v_fmamk_f32 v209, v209, 0xc0b8aa3b, v198
	v_fmamk_f32 v210, v210, 0xc0b8aa3b, v198
	v_fmamk_f32 v211, v211, 0xc0b8aa3b, v198
	v_mul_f32_e32 v204, v204, v144
	v_mul_f32_e32 v205, v205, v145
	v_mul_f32_e32 v206, v206, v146
	v_mul_f32_e32 v207, v207, v147
	v_fma_f32 v144, v200, v208, v204
	v_fma_f32 v145, v201, v209, v205
	v_fma_f32 v146, v202, v210, v206
	v_fma_f32 v147, v203, v211, v207
	v_exp_f32_e32 v200, v144
	v_exp_f32_e32 v201, v145
	v_exp_f32_e32 v202, v146
	v_exp_f32_e32 v203, v147
	v_add_f32_e32 v200, 1.0, v200
	v_add_f32_e32 v201, 1.0, v201
	v_add_f32_e32 v202, 1.0, v202
	v_add_f32_e32 v203, 1.0, v203
	v_rcp_f32_e32 v200, v200
	v_rcp_f32_e32 v201, v201
	v_rcp_f32_e32 v202, v202
	v_rcp_f32_e32 v203, v203
	v_fma_f32 v200, v200, 2.0, -1.0
	v_fma_f32 v201, v201, 2.0, -1.0
	v_fma_f32 v202, v202, 2.0, -1.0
	v_fma_f32 v203, v203, 2.0, -1.0
	v_mul_f32_e32 v216, v212, v200
	v_mul_f32_e32 v217, v213, v201
	v_mul_f32_e32 v218, v214, v202
	v_mul_f32_e32 v219, v215, v203
	v_mul_f32_e32 v236, v216, v228
	v_mul_f32_e32 v237, v216, v232
	v_fmac_f32_e32 v236, v217, v229
	v_fmac_f32_e32 v237, v217, v233
	v_fmac_f32_e32 v236, v218, v230
	v_fmac_f32_e32 v237, v218, v234
	v_fmac_f32_e32 v236, v219, v231
	v_fmac_f32_e32 v237, v219, v235
	v_mov_b32_e32 v238, v236
	v_mov_b32_e32 v239, v236
	v_mov_b32_e32 v240, v237
	v_mov_b32_e32 v241, v237
	s_nop 1
	v_permlane32_swap_b32_e32 v238, v239
	v_permlane32_swap_b32_e32 v240, v241
	v_add_f32_e32 v238, v238, v239
	v_add_f32_e32 v239, v240, v241
	ds_write_b64 v248, v[238:239] offset:1024
	v_cvt_pk_f16_f32 v220, v216, v217
	v_cvt_pk_f16_f32 v221, v218, v219
	v_exp_f32_e32 v200, v80
	v_exp_f32_e32 v201, v81
	v_exp_f32_e32 v202, v82
	v_exp_f32_e32 v203, v83
	v_exp_f32_e32 v204, v84
	v_exp_f32_e32 v205, v85
	v_exp_f32_e32 v206, v86
	v_exp_f32_e32 v207, v87
	v_exp_f32_e32 v208, v88
	v_exp_f32_e32 v209, v89
	v_exp_f32_e32 v210, v90
	v_exp_f32_e32 v211, v91
	v_exp_f32_e32 v212, v92
	v_exp_f32_e32 v213, v93
	v_exp_f32_e32 v214, v94
	v_exp_f32_e32 v215, v95
	v_add_f32_e32 v200, 1.0, v200
	v_add_f32_e32 v201, 1.0, v201
	v_add_f32_e32 v202, 1.0, v202
	v_add_f32_e32 v203, 1.0, v203
	v_add_f32_e32 v204, 1.0, v204
	v_add_f32_e32 v205, 1.0, v205
	v_add_f32_e32 v206, 1.0, v206
	v_add_f32_e32 v207, 1.0, v207
	v_add_f32_e32 v208, 1.0, v208
	v_add_f32_e32 v209, 1.0, v209
	v_add_f32_e32 v210, 1.0, v210
	v_add_f32_e32 v211, 1.0, v211
	v_add_f32_e32 v212, 1.0, v212
	v_add_f32_e32 v213, 1.0, v213
	v_add_f32_e32 v214, 1.0, v214
	v_add_f32_e32 v215, 1.0, v215
	v_rcp_f32_e32 v200, v200
	v_rcp_f32_e32 v201, v201
	v_rcp_f32_e32 v202, v202
	v_rcp_f32_e32 v203, v203
	v_rcp_f32_e32 v204, v204
	v_rcp_f32_e32 v205, v205
	v_rcp_f32_e32 v206, v206
	v_rcp_f32_e32 v207, v207
	v_rcp_f32_e32 v208, v208
	v_rcp_f32_e32 v209, v209
	v_rcp_f32_e32 v210, v210
	v_rcp_f32_e32 v211, v211
	v_rcp_f32_e32 v212, v212
	v_rcp_f32_e32 v213, v213
	v_rcp_f32_e32 v214, v214
	v_rcp_f32_e32 v215, v215
	v_fmamk_f32 v208, v208, 0xc0b8aa3b, v198
	v_fmamk_f32 v209, v209, 0xc0b8aa3b, v198
	v_fmamk_f32 v210, v210, 0xc0b8aa3b, v198
	v_fmamk_f32 v211, v211, 0xc0b8aa3b, v198
	v_mul_f32_e32 v204, v204, v148
	v_mul_f32_e32 v205, v205, v149
	v_mul_f32_e32 v206, v206, v150
	v_mul_f32_e32 v207, v207, v151
	v_fma_f32 v148, v200, v208, v204
	v_fma_f32 v149, v201, v209, v205
	v_fma_f32 v150, v202, v210, v206
	v_fma_f32 v151, v203, v211, v207
	v_exp_f32_e32 v200, v148
	v_exp_f32_e32 v201, v149
	v_exp_f32_e32 v202, v150
	v_exp_f32_e32 v203, v151
	v_add_f32_e32 v200, 1.0, v200
	v_add_f32_e32 v201, 1.0, v201
	v_add_f32_e32 v202, 1.0, v202
	v_add_f32_e32 v203, 1.0, v203
	v_rcp_f32_e32 v200, v200
	v_rcp_f32_e32 v201, v201
	v_rcp_f32_e32 v202, v202
	v_rcp_f32_e32 v203, v203
	v_fma_f32 v200, v200, 2.0, -1.0
	v_fma_f32 v201, v201, 2.0, -1.0
	v_fma_f32 v202, v202, 2.0, -1.0
	v_fma_f32 v203, v203, 2.0, -1.0
	v_mul_f32_e32 v216, v212, v200
	v_mul_f32_e32 v217, v213, v201
	v_mul_f32_e32 v218, v214, v202
	v_mul_f32_e32 v219, v215, v203
	v_mul_f32_e32 v236, v216, v228
	v_mul_f32_e32 v237, v216, v232
	v_fmac_f32_e32 v236, v217, v229
	v_fmac_f32_e32 v237, v217, v233
	v_fmac_f32_e32 v236, v218, v230
	v_fmac_f32_e32 v237, v218, v234
	v_fmac_f32_e32 v236, v219, v231
	v_fmac_f32_e32 v237, v219, v235
	v_mov_b32_e32 v238, v236
	v_mov_b32_e32 v239, v236
	v_mov_b32_e32 v240, v237
	v_mov_b32_e32 v241, v237
	s_nop 1
	v_permlane32_swap_b32_e32 v238, v239
	v_permlane32_swap_b32_e32 v240, v241
	v_add_f32_e32 v238, v238, v239
	v_add_f32_e32 v239, v240, v241
	ds_write_b64 v248, v[238:239] offset:1280
	v_cvt_pk_f16_f32 v222, v216, v217
	v_cvt_pk_f16_f32 v223, v218, v219
	s_nop 1
	v_permlane32_swap_b32_e32 v220, v222
	v_permlane32_swap_b32_e32 v221, v223
	s_cmp_eq_u32 s31, 0
	s_cbranch_scc1 .LD_slow8
	global_store_dwordx4 v195, v[220:223], s[36:37] offset:0
.LD_join9:
	s_lshl_b32 s64, s33, 19
	s_add_u32 s72, s62, s64
	s_addc_u32 s73, s63, 0
	s_waitcnt vmcnt(2)
	s_waitcnt vmcnt(1)
	s_waitcnt vmcnt(0)
	s_waitcnt lgkmcnt(0)
	s_barrier
	v_mov_b32_e32 v199, 3
	s_cmp_eq_u32 s31, 0
	s_cbranch_scc1 .LD_slow10
	global_store_dword v197, v199, s[40:41]
.LD_join11:
	ds_read_b64 v[200:201], v249 offset:0
	ds_read_b64 v[202:203], v249 offset:2048
	ds_read_b64 v[204:205], v249 offset:4096
	ds_read_b64 v[206:207], v249 offset:6144
	s_waitcnt lgkmcnt(0)
	v_add_f32_e32 v200, v200, v202
	v_add_f32_e32 v201, v201, v203
	v_add_f32_e32 v200, v200, v204
	v_add_f32_e32 v201, v201, v205
	v_add_f32_e32 v200, v200, v206
	v_add_f32_e32 v201, v201, v207
	global_store_dwordx2 v250, v[200:201], s[72:73]
	s_lshl_b32 s64, s33, 19
	s_add_u32 s64, s64, 0x200
	s_add_u32 s72, s62, s64
	s_addc_u32 s73, s63, 0
	ds_read_b64 v[200:201], v249 offset:512
	ds_read_b64 v[202:203], v249 offset:2560
	ds_read_b64 v[204:205], v249 offset:4608
	ds_read_b64 v[206:207], v249 offset:6656
	s_waitcnt lgkmcnt(0)
	v_add_f32_e32 v200, v200, v202
	v_add_f32_e32 v201, v201, v203
	v_add_f32_e32 v200, v200, v204
	v_add_f32_e32 v201, v201, v205
	v_add_f32_e32 v200, v200, v206
	v_add_f32_e32 v201, v201, v207
	global_store_dwordx2 v250, v[200:201], s[72:73]
	s_nop 1
	s_lshl_b32 s64, s33, 19
	s_add_u32 s64, s64, 0x400
	s_add_u32 s72, s62, s64
	s_addc_u32 s73, s63, 0
	ds_read_b64 v[200:201], v249 offset:1024
	ds_read_b64 v[202:203], v249 offset:3072
	ds_read_b64 v[204:205], v249 offset:5120
	ds_read_b64 v[206:207], v249 offset:7168
	s_waitcnt lgkmcnt(0)
	v_add_f32_e32 v200, v200, v202
	v_add_f32_e32 v201, v201, v203
	v_add_f32_e32 v200, v200, v204
	v_add_f32_e32 v201, v201, v205
	v_add_f32_e32 v200, v200, v206
	v_add_f32_e32 v201, v201, v207
	global_store_dwordx2 v250, v[200:201], s[72:73]
	s_nop 1
	s_mov_b32 s33, 1
	s_add_u32 s46, s42, 0x0
	s_addc_u32 s47, s43, 0
	global_load_dwordx4 v[0:3], v192, s[46:47] offset:0
	global_load_dwordx4 v[4:7], v192, s[46:47] offset:1024
	global_load_dwordx4 v[8:11], v192, s[46:47] offset:2048
	global_load_dwordx4 v[12:15], v192, s[46:47] offset:3072
	s_add_u32 s46, s42, 0x1000
	s_addc_u32 s47, s43, 0
	global_load_dwordx4 v[16:19], v192, s[46:47] offset:0
	global_load_dwordx4 v[20:23], v192, s[46:47] offset:1024
	global_load_dwordx4 v[24:27], v192, s[46:47] offset:2048
	global_load_dwordx4 v[28:31], v192, s[46:47] offset:3072
	s_add_u32 s46, s42, 0x2000
	s_addc_u32 s47, s43, 0
	global_load_dwordx4 v[32:35], v192, s[46:47] offset:0
	global_load_dwordx4 v[36:39], v192, s[46:47] offset:1024
	global_load_dwordx4 v[40:43], v192, s[46:47] offset:2048
	global_load_dwordx4 v[44:47], v192, s[46:47] offset:3072
	s_add_u32 s46, s42, 0x3000
	s_addc_u32 s47, s43, 0
	global_load_dwordx4 v[48:51], v192, s[46:47] offset:0
	global_load_dwordx4 v[52:55], v192, s[46:47] offset:1024
	global_load_dwordx4 v[56:59], v192, s[46:47] offset:2048
	global_load_dwordx4 v[60:63], v192, s[46:47] offset:3072
	s_waitcnt vmcnt(0)
	s_waitcnt lgkmcnt(0)
	s_cmp_ge_u32 s33, s28
	s_cbranch_scc1 .LD_end13
	s_sub_u32 s71, s33, 1
	s_and_b32 s64, s71, 1
	s_lshl_b32 s64, s64, 22
	s_add_u32 s64, s64, s49
	s_add_u32 s34, s6, s64
	s_addc_u32 s35, s7, 0
	s_lshl_b32 s64, s71, 3
	s_add_u32 s64, s64, s29
	s_lshl_b32 s64, s64, 7
	s_add_u32 s38, s8, s64
	s_addc_u32 s39, s9, 0
